# attention layers 0-2 tile loop: K/V LDS-DMA addresses via SGPR base + per-lane 32-bit offsets, softmax row-sum kept per lane and reduced once per q-block, dropped redundant max/add
# speedup vs baseline: 1.0111x; 1.0025x over previous
.LBB0_1247:
	v_readlane_b32 s0, v251, 54
	v_readlane_b32 s1, v251, 55
	s_andn2_b64 vcc, exec, s[0:1]
	v_readfirstlane_b32 s0, v219
	s_waitcnt lgkmcnt(0)
	s_barrier
	s_cbranch_vccnz .LBB0_1263
	v_bfe_u32 v3, v219, 4, 2
	v_lshrrev_b32_e32 v2, 4, v219
	v_lshlrev_b32_e32 v0, 3, v3
	v_mov_b32_e32 v1, v33
	v_lshlrev_b32_e32 v170, 2, v3
	v_lshl_add_u64 v[172:173], s[4:5], 0, v[0:1]
	v_bitop3_b32 v1, v2, v166, 3 bitop3:0x6c
	s_waitcnt vmcnt(14)
	v_lshrrev_b32_e32 v4, 2, v219
	v_or_b32_e32 v5, v170, v163
	v_lshlrev_b32_e32 v222, 4, v1
	v_bitop3_b32 v1, v3, v166, 4 bitop3:0x36
	v_and_or_b32 v4, v4, 4, v163
	v_lshlrev_b32_e32 v5, 8, v5
	v_and_b32_e32 v6, 8, v220
	v_lshlrev_b32_e32 v223, 4, v1
	v_bitop3_b32 v1, v3, v166, 8 bitop3:0x36
	v_lshlrev_b32_e32 v4, 1, v4
	v_add3_u32 v221, 0, v5, v6
	v_bfe_u32 v5, v219, 1, 1
	v_lshlrev_b32_e32 v224, 4, v1
	v_bitop3_b32 v1, v3, v166, 12 bitop3:0x36
	v_lshlrev_b32_e32 v225, 4, v1
	v_or_b32_e32 v1, v4, v5
	v_lshlrev_b32_e32 v237, 4, v1
	v_bitop3_b32 v1, v4, v5, 2 bitop3:0x1e
	v_lshlrev_b32_e32 v238, 4, v1
	v_bitop3_b32 v1, v4, v5, 4 bitop3:0x1e
	v_lshlrev_b32_e32 v239, 4, v1
	v_bitop3_b32 v1, v4, v5, 6 bitop3:0x1e
	v_lshlrev_b32_e32 v240, 4, v1
	v_bitop3_b32 v1, v4, v5, 8 bitop3:0x1e
	v_lshlrev_b32_e32 v241, 4, v1
	v_bitop3_b32 v1, v4, v5, 10 bitop3:0x1e
	v_lshlrev_b32_e32 v242, 4, v1
	v_bitop3_b32 v1, v4, v5, 12 bitop3:0x1e
	s_ashr_i32 s14, s0, 6
	v_lshlrev_b32_e32 v243, 4, v1
	v_bitop3_b32 v1, v4, v5, 14 bitop3:0x1e
	s_lshl_b32 s15, s14, 3
	v_lshlrev_b32_e32 v244, 4, v1
	v_or_b32_e32 v1, s15, v3
	v_lshlrev_b32_e32 v4, 3, v166
	v_lshlrev_b32_e32 v5, 4, v3
	s_and_b32 s20, s0, 0xffffff80
	s_lshl_b32 s0, s14, 5
	v_xor_b32_e32 v4, v5, v4
	v_or_b32_e32 v5, 4, v1
	v_and_or_b32 v245, s0, 32, v166
	v_mad_i64_i32 v[180:181], s[0:1], v1, s96, 0
	v_mad_i64_i32 v[182:183], s[0:1], v5, s96, 0
	v_bitop3_b32 v1, v1, v219, 4 bitop3:0x36
	v_lshlrev_b32_e32 v1, 3, v1
	s_lshl_b32 s0, s14, 14
	v_bitop3_b32 v2, s15, v219, v3 bitop3:0x36
	v_and_b32_e32 v6, 0x78, v1
	v_lshlrev_b32_e32 v1, 1, v5
	s_and_b32 s0, s0, 0x4000
	s_lshl_b32 s16, s14, 11
	v_lshlrev_b32_e32 v2, 3, v2
	v_bitop3_b32 v1, v1, v166, 14 bitop3:0x6c
	s_add_i32 s0, s0, 0
	v_add_u32_e32 v174, 0x2000, v168
	v_add_u32_e32 v176, 0x4000, v168
	v_add_u32_e32 v178, 0x6000, v168
	v_and_b32_e32 v2, 0x78, v2
	s_add_i32 s21, s16, 0
	s_waitcnt vmcnt(13)
	v_lshlrev_b32_e32 v8, 3, v1
	s_add_i32 s0, s0, 0x10000
	s_addk_i32 s15, 0x44
	v_lshl_add_u32 v171, v166, 8, 0
	v_ashrrev_i32_e32 v169, 31, v168
	v_ashrrev_i32_e32 v175, 31, v174
	v_ashrrev_i32_e32 v177, 31, v176
	v_ashrrev_i32_e32 v179, 31, v178
	v_lshl_add_u32 v246, v166, 9, s0
	v_or_b32_e32 v247, s15, v3
	v_lshlrev_b32_e32 v32, 1, v2
	v_lshlrev_b32_e32 v184, 1, v4
	v_lshlrev_b32_e32 v186, 1, v6
	v_lshlrev_b32_e32 v188, 1, v8
	v_add3_u32 v32, v180, v32, s84
	v_add3_u32 v184, v180, v184, s90
	v_add3_u32 v186, v182, v186, s84
	v_add3_u32 v188, v182, v188, s90
	v_lshlrev_b32_e32 v190, 1, v0
	s_add_i32 s22, s21, 0x8400
	s_mov_b32 s23, s83
	s_branch .LBB0_1250

.LBB0_1250:
	s_and_b32 s0, s23, 3
	s_lshl_b32 s1, s23, 10
	s_and_b32 s28, s1, 0x1000
	s_lshl_b32 s1, s0, 9
	s_ashr_i32 s26, s23, 3
	s_add_i32 s14, s1, s20
	s_sub_i32 s27, 63, s26
	s_ashr_i32 s15, s14, 31
	s_mul_i32 s1, s28, 0x9000
	s_add_u32 s1, s2, s1
	s_addc_u32 s16, s3, 0
	s_lshl_b32 s0, s0, 8
	s_add_u32 s0, s1, s0
	s_addc_u32 s1, s16, 0
	v_lshl_add_u64 v[192:193], s[14:15], 1, v[172:173]
	s_mov_b64 s[16:17], -1
	s_lshl_b64 s[14:15], s[14:15], 1
	s_branch .LBB0_1252

.LBB0_1252:
	s_and_b64 s[18:19], s[16:17], exec
	s_cselect_b32 s29, s26, s27
	s_lshl_b32 s18, s29, 6
	s_add_i32 s18, s18, s28
	v_or_b32_e32 v214, s18, v245
	v_mov_b64_e32 v[0:1], s[2:3]
	v_mad_i64_i32 v[2:3], s[30:31], v214, s96, v[0:1]
	v_lshl_add_u64 v[2:3], v[2:3], 0, s[14:15]
	v_mov_b32_e32 v191, v33
	v_or_b32_e32 v212, 16, v214
	v_lshl_add_u64 v[2:3], v[2:3], 0, v[190:191]
	s_mov_b64 s[34:35], 0x5000
	v_mad_i64_i32 v[0:1], s[30:31], v212, s96, v[0:1]
	v_lshl_add_u64 v[4:5], v[2:3], 0, s[34:35]
	v_add_co_u32_e32 v2, vcc, 0x5000, v2
	v_lshl_add_u64 v[0:1], v[0:1], 0, s[14:15]
	s_nop 0
	v_addc_co_u32_e32 v3, vcc, 0, v3, vcc
	v_lshl_add_u64 v[0:1], v[0:1], 0, v[190:191]
	s_mov_b32 m0, s21
	global_load_dwordx4 v[70:73], v[4:5], off offset:64
	global_load_dwordx4 v[74:77], v[4:5], off offset:128
	global_load_dwordx4 v[78:81], v[2:3], off
	global_load_dwordx4 v[82:85], v[4:5], off offset:192
	v_lshl_add_u64 v[2:3], v[0:1], 0, s[34:35]
	v_add_co_u32_e32 v0, vcc, 0x5000, v0
	s_ashr_i32 s19, s18, 31
	s_nop 0
	v_addc_co_u32_e32 v1, vcc, 0, v1, vcc
	global_load_dwordx4 v[86:89], v[2:3], off offset:64
	global_load_dwordx4 v[90:93], v[2:3], off offset:128
	global_load_dwordx4 v[94:97], v[0:1], off
	global_load_dwordx4 v[98:101], v[2:3], off offset:192
	s_barrier
	global_load_lds_dwordx4 v32, s[0:1]
	s_add_i32 m0, s21, 0x8000
	s_lshl_b64 s[18:19], s[18:19], 9
	global_load_lds_dwordx4 v184, s[0:1]
	s_add_i32 m0, s21, 0x400
	s_add_u32 s18, s24, s18
	s_addc_u32 s19, s25, s19
	v_lshl_add_u64 v[0:1], s[18:19], 0, v[168:169]
	v_lshl_add_u64 v[2:3], s[18:19], 0, v[174:175]
	global_load_dwordx4 v[24:27], v[0:1], off
	global_load_dwordx4 v[28:31], v[2:3], off
	v_lshl_add_u64 v[0:1], s[18:19], 0, v[176:177]
	v_lshl_add_u64 v[2:3], s[18:19], 0, v[178:179]
	global_load_dwordx4 v[38:41], v[0:1], off
	global_load_dwordx4 v[42:45], v[2:3], off
	s_waitcnt vmcnt(0)
	v_add_u32_e32 v46, 0, v168
	global_load_lds_dwordx4 v186, s[0:1]
	s_mov_b32 m0, s22
	v_add_u32_e32 v46, 0x10000, v46
	global_load_lds_dwordx4 v188, s[0:1]
	s_add_u32 s100, s0, 0x240000
	s_addc_u32 s101, s1, 0
	v_mov_b32_e32 v3, 0
	v_mov_b32_e32 v2, 0
	v_mov_b32_e32 v1, 0
	v_mov_b32_e32 v0, 0
	v_mov_b32_e32 v7, 0
	v_mov_b32_e32 v6, 0
	v_mov_b32_e32 v5, 0
	v_mov_b32_e32 v4, 0
	v_mov_b32_e32 v11, 0
	v_mov_b32_e32 v10, 0
	v_mov_b32_e32 v9, 0
	v_mov_b32_e32 v8, 0
	v_mov_b32_e32 v15, 0
	v_mov_b32_e32 v14, 0
	v_mov_b32_e32 v13, 0
	v_mov_b32_e32 v12, 0
	v_mov_b32_e32 v19, 0
	v_mov_b32_e32 v18, 0
	v_mov_b32_e32 v17, 0
	v_mov_b32_e32 v16, 0
	v_mov_b32_e32 v23, 0
	v_mov_b32_e32 v22, 0
	v_mov_b32_e32 v21, 0
	v_mov_b32_e32 v20, 0
	s_cmp_lt_i32 s29, 0
	v_mov_b32_e32 v49, 0
	v_mov_b32_e32 v48, 0
	v_mov_b32_e32 v47, 0
	v_mov_b32_e32 v53, 0
	v_mov_b32_e32 v52, 0
	v_mov_b32_e32 v51, 0
	v_mov_b32_e32 v50, 0
	v_mov_b32_e32 v57, 0
	v_mov_b32_e32 v56, 0
	v_mov_b32_e32 v55, 0
	v_mov_b32_e32 v54, 0
	v_mov_b32_e32 v61, 0
	v_mov_b32_e32 v60, 0
	v_mov_b32_e32 v59, 0
	v_mov_b32_e32 v58, 0
	v_mov_b32_e32 v65, 0
	ds_write_b128 v46, v[24:27]
	ds_write_b128 v46, v[28:31] offset:8192
	ds_write_b128 v46, v[38:41] offset:16384
	ds_write_b128 v46, v[42:45] offset:24576
	s_waitcnt vmcnt(0)
	v_mov_b32_e32 v27, 0
	v_mov_b32_e32 v26, 0
	v_mov_b32_e32 v25, 0
	v_mov_b32_e32 v24, 0
	v_mov_b32_e32 v31, 0
	v_mov_b32_e32 v30, 0
	v_mov_b32_e32 v29, 0
	v_mov_b32_e32 v28, 0
	v_mov_b32_e32 v41, 0
	v_mov_b32_e32 v40, 0
	v_mov_b32_e32 v39, 0
	v_mov_b32_e32 v38, 0
	v_mov_b32_e32 v45, 0
	v_mov_b32_e32 v44, 0
	v_mov_b32_e32 v43, 0
	v_mov_b32_e32 v42, 0
	v_mov_b32_e32 v46, 0
	v_mov_b32_e32 v64, 0
	v_mov_b32_e32 v63, 0
	v_mov_b32_e32 v62, 0
	v_mov_b32_e32 v69, 0
	v_mov_b32_e32 v68, 0
	v_mov_b32_e32 v67, 0
	v_mov_b32_e32 v66, 0
	v_mov_b32_e32 v102, 0
	v_mov_b32_e32 v103, 0
	s_waitcnt vmcnt(0) lgkmcnt(0)
	s_barrier
	s_cbranch_scc1 .LBB0_1251
	v_mov_b32_e32 v66, v33
	v_mov_b32_e32 v67, v33
	v_mov_b32_e32 v68, v33
	v_mov_b32_e32 v69, v33
	v_mov_b64_e32 v[62:63], v[66:67]
	v_mov_b64_e32 v[58:59], v[66:67]
	v_mov_b64_e32 v[54:55], v[66:67]
	v_mov_b64_e32 v[50:51], v[66:67]
	v_mov_b64_e32 v[46:47], v[66:67]
	v_mov_b64_e32 v[42:43], v[66:67]
	v_mov_b64_e32 v[38:39], v[66:67]
	v_mov_b64_e32 v[28:29], v[66:67]
	v_mov_b64_e32 v[24:25], v[66:67]
	v_mov_b64_e32 v[20:21], v[66:67]
	v_mov_b64_e32 v[16:17], v[66:67]
	v_mov_b64_e32 v[12:13], v[66:67]
	v_mov_b64_e32 v[8:9], v[66:67]
	v_mov_b64_e32 v[4:5], v[66:67]
	v_mov_b64_e32 v[0:1], v[66:67]
	s_add_i32 s30, s29, 1
	s_mov_b32 s31, 0
	v_mov_b32_e32 v218, 0xf149f2ca
	v_mov_b32_e32 v215, 0
	v_mov_b32_e32 v213, v246
	v_mov_b32_e32 v248, 0
	v_mov_b32_e32 v167, 0xf149f2ca
	v_mov_b64_e32 v[64:65], v[68:69]
	v_mov_b64_e32 v[60:61], v[68:69]
	v_mov_b64_e32 v[56:57], v[68:69]
	v_mov_b64_e32 v[52:53], v[68:69]
	v_mov_b64_e32 v[48:49], v[68:69]
	v_mov_b64_e32 v[44:45], v[68:69]
	v_mov_b64_e32 v[40:41], v[68:69]
	v_mov_b64_e32 v[30:31], v[68:69]
	v_mov_b64_e32 v[26:27], v[68:69]
	v_mov_b64_e32 v[22:23], v[68:69]
	v_mov_b64_e32 v[18:19], v[68:69]
	v_mov_b64_e32 v[14:15], v[68:69]
	v_mov_b64_e32 v[10:11], v[68:69]
	v_mov_b64_e32 v[6:7], v[68:69]
	v_mov_b64_e32 v[2:3], v[68:69]
	s_and_b32 s34, s31, 1
	s_cmp_lt_i32 s31, s29
	s_mov_b64 s[18:19], -1
	s_cbranch_scc1 .LBB0_1256
	s_branch .LBB0_1255
.LBB0_1254:
	v_mov_b32_e32 v218, v187
	v_mov_b32_e32 v167, v249
	s_and_b32 s34, s31, 1
	s_cmp_lt_i32 s31, s29
	s_mov_b64 s[18:19], -1
	s_cbranch_scc1 .LBB0_1256

.LBB0_1256:
	s_andn2_b64 vcc, exec, s[18:19]
	s_cbranch_vccnz .LBB0_1258
	s_lshl_b32 s33, s34, 14
	s_xor_b32 s34, s33, 0x4000
	s_add_i32 s34, s21, s34
	s_mov_b32 m0, s34
	s_nop 0
	global_load_lds_dwordx4 v32, s[100:101]
	s_add_i32 m0, s34, 0x8000
	s_nop 0
	global_load_lds_dwordx4 v184, s[100:101]
	s_add_i32 m0, s34, 0x400
	s_nop 0
	global_load_lds_dwordx4 v186, s[100:101]
	s_add_i32 m0, s34, 0x8400
	s_nop 0
	global_load_lds_dwordx4 v188, s[100:101]
	s_add_u32 s100, s100, 0x240000
	s_addc_u32 s101, s101, 0
.LBB0_1258:
	v_add_u32_e32 v114, s33, v171
	v_add_u32_e32 v142, v114, v222
	ds_read_b128 v[102:105], v142
	v_add_u32_e32 v143, v114, v223
	ds_read_b128 v[106:109], v143
	v_add_u32_e32 v144, v114, v224
	ds_read_b128 v[110:113], v144
	v_add_u32_e32 v145, v114, v225
	ds_read_b128 v[114:117], v145
	ds_read_b128 v[118:121], v142 offset:4096
	ds_read_b128 v[122:125], v143 offset:4096
	ds_read_b128 v[126:129], v144 offset:4096
	ds_read_b128 v[130:133], v145 offset:4096
	s_waitcnt lgkmcnt(0)
	v_mfma_f32_16x16x32_bf16 v[138:141], v[118:121], v[78:81], 0
	v_add_u32_e32 v185, s33, v221
	v_mfma_f32_16x16x32_bf16 v[134:137], v[102:105], v[78:81], 0
	v_mfma_f32_16x16x32_bf16 v[102:105], v[102:105], v[94:97], 0
	v_mfma_f32_16x16x32_bf16 v[118:121], v[118:121], v[94:97], 0
	v_mfma_f32_16x16x32_bf16 v[134:137], v[106:109], v[70:73], v[134:137]
	v_mfma_f32_16x16x32_bf16 v[102:105], v[106:109], v[86:89], v[102:105]
	v_mfma_f32_16x16x32_bf16 v[138:141], v[122:125], v[70:73], v[138:141]
	v_mfma_f32_16x16x32_bf16 v[118:121], v[122:125], v[86:89], v[118:121]
	v_mfma_f32_16x16x32_bf16 v[134:137], v[110:113], v[74:77], v[134:137]
	v_mfma_f32_16x16x32_bf16 v[102:105], v[110:113], v[90:93], v[102:105]
	v_mfma_f32_16x16x32_bf16 v[138:141], v[126:129], v[74:77], v[138:141]
	v_mfma_f32_16x16x32_bf16 v[118:121], v[126:129], v[90:93], v[118:121]
	v_mfma_f32_16x16x32_bf16 v[162:165], v[114:117], v[82:85], v[134:137]
	v_mfma_f32_16x16x32_bf16 v[134:137], v[114:117], v[98:101], v[102:105]
	s_nop 3
	ds_read_b128 v[102:105], v142 offset:8192
	ds_read_b128 v[106:109], v143 offset:8192
	ds_read_b128 v[110:113], v144 offset:8192
	ds_read_b128 v[114:117], v145 offset:8192
	v_max_f32_e32 v187, v164, v165
	v_mfma_f32_16x16x32_bf16 v[158:161], v[130:133], v[82:85], v[138:141]
	v_max3_f32 v187, v162, v163, v187
	v_mfma_f32_16x16x32_bf16 v[138:141], v[130:133], v[98:101], v[118:121]
	s_nop 2
	ds_read_b128 v[118:121], v142 offset:12288
	ds_read_b128 v[122:125], v143 offset:12288
	ds_read_b128 v[126:129], v144 offset:12288
	ds_read_b128 v[130:133], v145 offset:12288
	v_max3_f32 v189, v159, v160, v161
	v_max3_f32 v187, v187, v158, v189
	s_waitcnt lgkmcnt(0)
	v_mfma_f32_16x16x32_bf16 v[142:145], v[102:105], v[78:81], 0
	v_mfma_f32_16x16x32_bf16 v[102:105], v[102:105], v[94:97], 0
	v_mfma_f32_16x16x32_bf16 v[102:105], v[106:109], v[86:89], v[102:105]
	v_mfma_f32_16x16x32_bf16 v[102:105], v[110:113], v[90:93], v[102:105]
	v_mfma_f32_16x16x32_bf16 v[146:149], v[114:117], v[98:101], v[102:105]
	v_mfma_f32_16x16x32_bf16 v[102:105], v[118:121], v[78:81], 0
	v_mfma_f32_16x16x32_bf16 v[142:145], v[106:109], v[70:73], v[142:145]
	v_mfma_f32_16x16x32_bf16 v[102:105], v[122:125], v[70:73], v[102:105]
	v_mfma_f32_16x16x32_bf16 v[142:145], v[110:113], v[74:77], v[142:145]
	v_mfma_f32_16x16x32_bf16 v[102:105], v[126:129], v[74:77], v[102:105]
	v_mfma_f32_16x16x32_bf16 v[154:157], v[114:117], v[82:85], v[142:145]
	v_mfma_f32_16x16x32_bf16 v[150:153], v[130:133], v[82:85], v[102:105]
	v_mfma_f32_16x16x32_bf16 v[102:105], v[118:121], v[94:97], 0
	s_nop 5
	v_max3_f32 v189, v155, v156, v157
	v_max3_f32 v187, v187, v154, v189
	v_max3_f32 v189, v151, v152, v153
	v_mfma_f32_16x16x32_bf16 v[102:105], v[122:125], v[86:89], v[102:105]
	v_max3_f32 v187, v187, v150, v189
	v_mov_b32_e32 v189, v187
	s_nop 1
	v_permlane16_swap_b32_e32 v187, v189
	v_mfma_f32_16x16x32_bf16 v[102:105], v[126:129], v[90:93], v[102:105]
	v_max_f32 v187, v187, v189
	s_nop 0
	v_mov_b32_e32 v189, v187
	s_nop 1
	v_permlane32_swap_b32_e32 v187, v189
	v_max_f32 v187, v187, v189
	v_mfma_f32_16x16x32_bf16 v[142:145], v[130:133], v[98:101], v[102:105]
	v_mul_f32_e32 v187, 0x3e0293ee, v187
	v_add_f32_e32 v189, 0x41000000, v218
	v_cmp_gt_f32_e32 vcc, v187, v189
	v_add_u32_e32 v102, v185, v237
	ds_read_b64_tr_b16 v[130:131], v102 offset:32768
	ds_read_b64_tr_b16 v[132:133], v102 offset:36864
	ds_read_b64_tr_b16 v[122:123], v102 offset:40960
	ds_read_b64_tr_b16 v[124:125], v102 offset:45056
	v_add_u32_e32 v102, v185, v238
	ds_read_b64_tr_b16 v[126:127], v102 offset:32768
	ds_read_b64_tr_b16 v[128:129], v102 offset:36864
	ds_read_b64_tr_b16 v[114:115], v102 offset:40960
	ds_read_b64_tr_b16 v[116:117], v102 offset:45056
	v_add_u32_e32 v102, v185, v239
	v_add_u32_e32 v104, v185, v240
	v_cndmask_b32_e32 v187, v218, v187, vcc
	ds_read_b64_tr_b16 v[118:119], v102 offset:32768
	ds_read_b64_tr_b16 v[120:121], v102 offset:36864
	ds_read_b64_tr_b16 v[110:111], v102 offset:40960
	ds_read_b64_tr_b16 v[112:113], v102 offset:45056
	ds_read_b64_tr_b16 v[106:107], v104 offset:32768
	ds_read_b64_tr_b16 v[108:109], v104 offset:36864
	ds_read_b64_tr_b16 v[102:103], v104 offset:40960
	ds_read_b64_tr_b16 v[104:105], v104 offset:45056
	ds_read_b64 v[198:199], v213
	v_fma_f32 v162, v162, s97, -v187
	v_exp_f32_e32 v162, v162
	v_fma_f32 v163, v163, s97, -v187
	v_exp_f32_e32 v163, v163
	v_fma_f32 v164, v164, s97, -v187
	v_exp_f32_e32 v164, v164
	v_fma_f32 v165, v165, s97, -v187
	v_exp_f32_e32 v165, v165
	v_fma_f32 v158, v158, s97, -v187
	s_waitcnt lgkmcnt(0)
	v_lshrrev_b64 v[216:217], v170, v[198:199]
	v_bfe_i32 v198, v216, 0, 1
	v_exp_f32_e32 v158, v158
	v_and_b32_e32 v162, v198, v162
	v_fma_f32 v159, v159, s97, -v187
	v_bfe_i32 v199, v216, 1, 1
	v_and_b32_e32 v163, v199, v163
	v_exp_f32_e32 v159, v159
	v_fma_f32 v160, v160, s97, -v187
	v_add_f32_e32 v198, v162, v163
	v_bfe_i32 v199, v216, 2, 1
	v_exp_f32_e32 v160, v160
	v_and_b32_e32 v164, v199, v164
	v_fma_f32 v161, v161, s97, -v187
	v_bfe_i32 v200, v216, 3, 1
	v_add_f32_e32 v198, v198, v164
	v_and_b32_e32 v165, v200, v165
	v_exp_f32_e32 v161, v161
	v_fma_f32 v154, v154, s97, -v187
	v_add_f32_e32 v198, v198, v165
	v_bfe_i32 v199, v216, 16, 1
	v_exp_f32_e32 v154, v154
	v_and_b32_e32 v158, v199, v158
	v_fma_f32 v155, v155, s97, -v187
	v_bfe_i32 v200, v216, 17, 1
	v_add_f32_e32 v198, v198, v158
	v_and_b32_e32 v159, v200, v159
	v_exp_f32_e32 v155, v155
	v_fma_f32 v156, v156, s97, -v187
	v_add_f32_e32 v198, v198, v159
	v_bfe_i32 v199, v216, 18, 1
	v_exp_f32_e32 v156, v156
	v_and_b32_e32 v160, v199, v160
	v_fma_f32 v157, v157, s97, -v187
	v_bfe_i32 v200, v216, 19, 1
	v_add_f32_e32 v198, v198, v160
	v_and_b32_e32 v161, v200, v161
	v_exp_f32_e32 v157, v157
	v_add_f32_e32 v198, v198, v161
	v_bfe_i32 v199, v217, 0, 1
	v_fma_f32 v150, v150, s97, -v187
	v_and_b32_e32 v154, v199, v154
	v_bfe_i32 v200, v217, 1, 1
	v_add_f32_e32 v198, v198, v154
	v_and_b32_e32 v155, v200, v155
	v_exp_f32_e32 v150, v150
	v_fma_f32 v151, v151, s97, -v187
	v_add_f32_e32 v198, v198, v155
	v_bfe_i32 v199, v217, 2, 1
	v_exp_f32_e32 v151, v151
	v_and_b32_e32 v216, v199, v156
	v_fma_f32 v152, v152, s97, -v187
	v_bfe_i32 v200, v217, 3, 1
	v_add_f32_e32 v156, v198, v216
	v_and_b32_e32 v157, v200, v157
	v_exp_f32_e32 v152, v152
	v_fma_f32 v153, v153, s97, -v187
	v_add_f32_e32 v198, v156, v157
	v_bfe_i32 v156, v217, 16, 1
	v_exp_f32_e32 v153, v153
	v_and_b32_e32 v156, v156, v150
	v_bfe_i32 v199, v217, 17, 1
	v_add_f32_e32 v150, v198, v156
	v_and_b32_e32 v151, v199, v151
	v_add_f32_e32 v150, v150, v151
	v_bfe_i32 v198, v217, 18, 1
	v_sub_f32_e32 v189, v218, v187
	v_and_b32_e32 v152, v198, v152
	v_bfe_i32 v199, v217, 19, 1
	v_add_f32_e32 v150, v150, v152
	v_and_b32_e32 v153, v199, v153
	v_add_f32_e32 v198, v150, v153
	v_exp_f32_e32 v150, v189
	s_nop 0
	v_cmp_eq_f32_e32 vcc, 1.0, v150
	v_fma_f32 v215, v215, v150, v198
	s_cmp_eq_u64 vcc, exec
	s_cbranch_scc1 .LBB0_1260
	v_pk_mul_f32 v[68:69], v[68:69], v[150:151] op_sel_hi:[1,0]
	v_pk_mul_f32 v[66:67], v[66:67], v[150:151] op_sel_hi:[1,0]
	v_pk_mul_f32 v[64:65], v[64:65], v[150:151] op_sel_hi:[1,0]
	v_pk_mul_f32 v[62:63], v[62:63], v[150:151] op_sel_hi:[1,0]
	v_pk_mul_f32 v[60:61], v[60:61], v[150:151] op_sel_hi:[1,0]
	v_pk_mul_f32 v[58:59], v[58:59], v[150:151] op_sel_hi:[1,0]
	v_pk_mul_f32 v[56:57], v[56:57], v[150:151] op_sel_hi:[1,0]
	v_pk_mul_f32 v[54:55], v[54:55], v[150:151] op_sel_hi:[1,0]
	v_pk_mul_f32 v[52:53], v[52:53], v[150:151] op_sel_hi:[1,0]
	v_pk_mul_f32 v[50:51], v[50:51], v[150:151] op_sel_hi:[1,0]
	v_pk_mul_f32 v[48:49], v[48:49], v[150:151] op_sel_hi:[1,0]
	v_pk_mul_f32 v[46:47], v[46:47], v[150:151] op_sel_hi:[1,0]
	v_pk_mul_f32 v[44:45], v[44:45], v[150:151] op_sel_hi:[1,0]
	v_pk_mul_f32 v[42:43], v[42:43], v[150:151] op_sel_hi:[1,0]
	v_pk_mul_f32 v[40:41], v[40:41], v[150:151] op_sel_hi:[1,0]
	v_pk_mul_f32 v[38:39], v[38:39], v[150:151] op_sel_hi:[1,0]
.LBB0_1260:
	v_max_f32_e32 v200, v136, v137
	v_max3_f32 v200, v134, v135, v200
	v_max3_f32 v201, v139, v140, v141
	v_max3_f32 v200, v200, v138, v201
	v_max3_f32 v201, v147, v148, v149
	v_max3_f32 v200, v200, v146, v201
	v_max3_f32 v201, v143, v144, v145
	v_max3_f32 v200, v200, v142, v201
	v_mov_b32_e32 v201, v200
	s_nop 1
	v_permlane16_swap_b32_e32 v200, v201
	v_max_f32 v200, v200, v201
	ds_read_b64 v[198:199], v213 offset:8192
	v_mov_b32_e32 v201, v200
	s_nop 1
	v_permlane32_swap_b32_e32 v200, v201
	v_max_f32 v200, v200, v201
	v_add_f32_e32 v201, 0x41000000, v167
	v_mul_f32_e32 v200, 0x3e0293ee, v200
	v_cmp_gt_f32_e32 vcc, v200, v201
	s_waitcnt lgkmcnt(0)
	v_lshrrev_b64 v[198:199], v170, v[198:199]
	v_bfe_i32 v201, v198, 0, 1
	v_cndmask_b32_e32 v249, v167, v200, vcc
	v_fma_f32 v135, v135, s97, -v249
	v_exp_f32_e32 v135, v135
	v_sub_f32_e32 v200, v167, v249
	v_bfe_i32 v167, v198, 1, 1
	v_fma_f32 v134, v134, s97, -v249
	v_and_b32_e32 v167, v167, v135
	v_fma_f32 v135, v136, s97, -v249
	v_fma_f32 v136, v137, s97, -v249
	v_exp_f32_e32 v134, v134
	v_exp_f32_e32 v136, v136
	v_exp_f32_e32 v137, v135
	v_bfe_i32 v135, v198, 3, 1
	v_and_b32_e32 v218, v201, v134
	v_bfe_i32 v201, v198, 2, 1
	v_and_b32_e32 v135, v135, v136
	v_and_b32_e32 v136, v201, v137
	v_fma_f32 v137, v138, s97, -v249
	v_fma_f32 v138, v139, s97, -v249
	v_exp_f32_e32 v138, v138
	v_exp_f32_e32 v139, v137
	v_bfe_i32 v137, v198, 17, 1
	v_bfe_i32 v201, v198, 16, 1
	v_and_b32_e32 v137, v137, v138
	v_and_b32_e32 v138, v201, v139
	v_fma_f32 v139, v140, s97, -v249
	v_fma_f32 v140, v141, s97, -v249
	v_exp_f32_e32 v140, v140
	v_exp_f32_e32 v141, v139
	v_bfe_i32 v139, v198, 19, 1
	v_bfe_i32 v201, v198, 18, 1
	v_add_f32_e32 v134, v218, v167
	v_and_b32_e32 v139, v139, v140
	v_and_b32_e32 v140, v201, v141
	v_fma_f32 v141, v146, s97, -v249
	v_fma_f32 v146, v147, s97, -v249
	v_exp_f32_e32 v146, v146
	v_exp_f32_e32 v147, v141
	v_add_f32_e32 v134, v134, v136
	v_add_f32_e32 v134, v134, v135
	v_bfe_i32 v141, v199, 1, 1
	v_add_f32_e32 v134, v134, v138
	v_bfe_i32 v198, v199, 0, 1
	v_and_b32_e32 v141, v141, v146
	v_and_b32_e32 v146, v198, v147
	v_fma_f32 v147, v148, s97, -v249
	v_fma_f32 v148, v149, s97, -v249
	v_add_f32_e32 v134, v134, v137
	v_exp_f32_e32 v148, v148
	v_exp_f32_e32 v149, v147
	v_add_f32_e32 v134, v134, v140
	v_fma_f32 v142, v142, s97, -v249
	v_add_f32_e32 v134, v134, v139
	v_fma_f32 v143, v143, s97, -v249
	v_exp_f32_e32 v142, v142
	v_add_f32_e32 v134, v134, v146
	v_bfe_i32 v147, v199, 3, 1
	v_exp_f32_e32 v143, v143
	v_fma_f32 v144, v144, s97, -v249
	v_add_f32_e32 v134, v134, v141
	v_bfe_i32 v198, v199, 2, 1
	v_and_b32_e32 v147, v147, v148
	v_and_b32_e32 v148, v198, v149
	v_fma_f32 v145, v145, s97, -v249
	v_exp_f32_e32 v144, v144
	v_add_f32_e32 v134, v134, v148
	v_exp_f32_e32 v145, v145
	v_add_f32_e32 v134, v134, v147
	v_bfe_i32 v149, v199, 16, 1
	v_bfe_i32 v198, v199, 17, 1
	s_nop 0
	v_and_b32_e32 v142, v149, v142
	v_and_b32_e32 v143, v198, v143
	v_add_f32_e32 v134, v134, v142
	v_add_f32_e32 v134, v134, v143
	v_bfe_i32 v149, v199, 18, 1
	v_bfe_i32 v198, v199, 19, 1
	s_nop 0
	v_and_b32_e32 v144, v149, v144
	v_and_b32_e32 v145, v198, v145
	v_add_f32_e32 v134, v134, v144
	v_add_f32_e32 v149, v134, v145
	v_exp_f32_e32 v134, v200
	s_nop 0
	v_cmp_eq_f32_e32 vcc, 1.0, v134
	v_fma_f32 v248, v248, v134, v149
	s_cmp_eq_u64 vcc, exec
	s_cbranch_scc1 .LBB0_1262
	v_pk_mul_f32 v[30:31], v[30:31], v[134:135] op_sel_hi:[1,0]
	v_pk_mul_f32 v[28:29], v[28:29], v[134:135] op_sel_hi:[1,0]
	v_pk_mul_f32 v[26:27], v[26:27], v[134:135] op_sel_hi:[1,0]
	v_pk_mul_f32 v[24:25], v[24:25], v[134:135] op_sel_hi:[1,0]
	v_pk_mul_f32 v[22:23], v[22:23], v[134:135] op_sel_hi:[1,0]
	v_pk_mul_f32 v[20:21], v[20:21], v[134:135] op_sel_hi:[1,0]
	v_pk_mul_f32 v[18:19], v[18:19], v[134:135] op_sel_hi:[1,0]
	v_pk_mul_f32 v[16:17], v[16:17], v[134:135] op_sel_hi:[1,0]
	v_pk_mul_f32 v[14:15], v[14:15], v[134:135] op_sel_hi:[1,0]
	v_pk_mul_f32 v[12:13], v[12:13], v[134:135] op_sel_hi:[1,0]
	v_pk_mul_f32 v[10:11], v[10:11], v[134:135] op_sel_hi:[1,0]
	v_pk_mul_f32 v[8:9], v[8:9], v[134:135] op_sel_hi:[1,0]
	v_pk_mul_f32 v[6:7], v[6:7], v[134:135] op_sel_hi:[1,0]
	v_pk_mul_f32 v[4:5], v[4:5], v[134:135] op_sel_hi:[1,0]
	v_pk_mul_f32 v[2:3], v[2:3], v[134:135] op_sel_hi:[1,0]
	v_pk_mul_f32 v[0:1], v[0:1], v[134:135] op_sel_hi:[1,0]
.LBB0_1262:
	v_cvt_pk_bf16_f32 v162, v162, v163
	v_cvt_pk_bf16_f32 v163, v164, v165
	v_cvt_pk_bf16_f32 v164, v158, v159
	v_cvt_pk_bf16_f32 v165, v160, v161
	v_cvt_pk_bf16_f32 v158, v218, v167
	v_cvt_pk_bf16_f32 v159, v136, v135
	v_cvt_pk_bf16_f32 v160, v138, v137
	v_cvt_pk_bf16_f32 v161, v140, v139
	v_mfma_f32_16x16x32_bf16 v[54:57], v[106:109], v[162:165], v[54:57]
	v_cvt_pk_bf16_f32 v154, v154, v155
	v_cvt_pk_bf16_f32 v155, v216, v157
	v_cvt_pk_bf16_f32 v156, v156, v151
	v_mfma_f32_16x16x32_bf16 v[16:19], v[106:109], v[158:161], v[16:19]
	v_cvt_pk_bf16_f32 v157, v152, v153
	v_add_u32_e32 v108, v185, v241
	s_add_i32 s31, s31, 1
	v_mfma_f32_16x16x32_bf16 v[66:69], v[130:133], v[162:165], v[66:69]
	v_add_u32_e32 v213, 8, v213
	s_cmp_eq_u32 s30, s31
	v_mfma_f32_16x16x32_bf16 v[28:31], v[130:133], v[158:161], v[28:31]
	v_cvt_pk_bf16_f32 v130, v146, v141
	v_cvt_pk_bf16_f32 v131, v148, v147
	v_cvt_pk_bf16_f32 v132, v142, v143
	v_cvt_pk_bf16_f32 v133, v144, v145
	v_mfma_f32_16x16x32_bf16 v[54:57], v[102:105], v[154:157], v[54:57]
	s_nop 0
	v_mfma_f32_16x16x32_bf16 v[16:19], v[102:105], v[130:133], v[16:19]
	ds_read_b64_tr_b16 v[102:103], v108 offset:32768
	ds_read_b64_tr_b16 v[104:105], v108 offset:36864
	ds_read_b64_tr_b16 v[106:107], v108 offset:40960
	ds_read_b64_tr_b16 v[108:109], v108 offset:45056
	v_mfma_f32_16x16x32_bf16 v[58:61], v[118:121], v[162:165], v[58:61]
	v_mfma_f32_16x16x32_bf16 v[20:23], v[118:121], v[158:161], v[20:23]
	s_waitcnt lgkmcnt(2)
	v_mfma_f32_16x16x32_bf16 v[50:53], v[102:105], v[162:165], v[50:53]
	v_mfma_f32_16x16x32_bf16 v[12:15], v[102:105], v[158:161], v[12:15]
	v_mfma_f32_16x16x32_bf16 v[58:61], v[110:113], v[154:157], v[58:61]
	v_mfma_f32_16x16x32_bf16 v[20:23], v[110:113], v[130:133], v[20:23]
	v_add_u32_e32 v110, v185, v242
	s_waitcnt lgkmcnt(0)
	v_mfma_f32_16x16x32_bf16 v[50:53], v[106:109], v[154:157], v[50:53]
	v_mfma_f32_16x16x32_bf16 v[12:15], v[106:109], v[130:133], v[12:15]
	ds_read_b64_tr_b16 v[102:103], v110 offset:32768
	ds_read_b64_tr_b16 v[104:105], v110 offset:36864
	ds_read_b64_tr_b16 v[106:107], v110 offset:40960
	ds_read_b64_tr_b16 v[108:109], v110 offset:45056
	v_add_u32_e32 v110, v185, v243
	s_waitcnt lgkmcnt(2)
	v_mfma_f32_16x16x32_bf16 v[46:49], v[102:105], v[162:165], v[46:49]
	v_mfma_f32_16x16x32_bf16 v[8:11], v[102:105], v[158:161], v[8:11]
	s_waitcnt lgkmcnt(0)
	v_mfma_f32_16x16x32_bf16 v[46:49], v[106:109], v[154:157], v[46:49]
	v_mfma_f32_16x16x32_bf16 v[8:11], v[106:109], v[130:133], v[8:11]
	ds_read_b64_tr_b16 v[102:103], v110 offset:32768
	ds_read_b64_tr_b16 v[104:105], v110 offset:36864
	ds_read_b64_tr_b16 v[106:107], v110 offset:40960
	ds_read_b64_tr_b16 v[108:109], v110 offset:45056
	s_waitcnt lgkmcnt(2)
	v_mfma_f32_16x16x32_bf16 v[42:45], v[102:105], v[162:165], v[42:45]
	v_mfma_f32_16x16x32_bf16 v[4:7], v[102:105], v[158:161], v[4:7]
	v_add_u32_e32 v103, v185, v244
	ds_read_b64_tr_b16 v[110:111], v103 offset:32768
	ds_read_b64_tr_b16 v[112:113], v103 offset:36864
	s_waitcnt lgkmcnt(2)
	v_mfma_f32_16x16x32_bf16 v[42:45], v[106:109], v[154:157], v[42:45]
	v_mfma_f32_16x16x32_bf16 v[4:7], v[106:109], v[130:133], v[4:7]
	ds_read_b64_tr_b16 v[104:105], v103 offset:40960
	ds_read_b64_tr_b16 v[106:107], v103 offset:45056
	s_waitcnt vmcnt(0)
	v_mfma_f32_16x16x32_bf16 v[62:65], v[126:129], v[162:165], v[62:65]
	s_waitcnt lgkmcnt(0)
	s_barrier
	v_mfma_f32_16x16x32_bf16 v[24:27], v[126:129], v[158:161], v[24:27]
	v_mfma_f32_16x16x32_bf16 v[38:41], v[110:113], v[162:165], v[38:41]
	v_mfma_f32_16x16x32_bf16 v[0:3], v[110:113], v[158:161], v[0:3]
	v_mfma_f32_16x16x32_bf16 v[66:69], v[122:125], v[154:157], v[66:69]
	v_mfma_f32_16x16x32_bf16 v[28:31], v[122:125], v[130:133], v[28:31]
	v_mfma_f32_16x16x32_bf16 v[62:65], v[114:117], v[154:157], v[62:65]
	v_mfma_f32_16x16x32_bf16 v[24:27], v[114:117], v[130:133], v[24:27]
	v_mfma_f32_16x16x32_bf16 v[38:41], v[104:107], v[154:157], v[38:41]
	v_mfma_f32_16x16x32_bf16 v[0:3], v[104:107], v[130:133], v[0:3]
	s_cbranch_scc0 .LBB0_1254
	v_mov_b32_e32 v189, v215
	v_mov_b32_e32 v198, v248
	s_nop 1
	v_permlane16_swap_b32_e32 v215, v189
	v_permlane16_swap_b32_e32 v248, v198
	v_add_f32_e32 v189, v215, v189
	v_add_f32_e32 v198, v248, v198
	v_mov_b32_e32 v217, v189
	v_mov_b32_e32 v250, v198
	s_nop 1
	v_permlane32_swap_b32_e32 v189, v217
	v_permlane32_swap_b32_e32 v198, v250
	v_add_f32_e32 v103, v189, v217
	v_add_f32_e32 v102, v198, v250
	s_branch .LBB0_1251

	.amdhsa_kernel _Z3fwd4Args
		.amdhsa_group_segment_fixed_size 0
		.amdhsa_private_segment_fixed_size 0
		.amdhsa_kernarg_size 440
		.amdhsa_user_sgpr_count 2
		.amdhsa_user_sgpr_dispatch_ptr 0
		.amdhsa_user_sgpr_queue_ptr 0
		.amdhsa_user_sgpr_kernarg_segment_ptr 1
		.amdhsa_user_sgpr_dispatch_id 0
		.amdhsa_user_sgpr_kernarg_preload_length 0
		.amdhsa_user_sgpr_kernarg_preload_offset 0
		.amdhsa_user_sgpr_private_segment_size 0
		.amdhsa_uses_dynamic_stack 0
		.amdhsa_enable_private_segment 0
		.amdhsa_system_sgpr_workgroup_id_x 1
		.amdhsa_system_sgpr_workgroup_id_y 0
		.amdhsa_system_sgpr_workgroup_id_z 0
		.amdhsa_system_sgpr_workgroup_info 0
		.amdhsa_system_vgpr_workitem_id 0
		.amdhsa_next_free_vgpr 256
		.amdhsa_next_free_sgpr 102
		.amdhsa_accum_offset 256
		.amdhsa_reserve_vcc 1
		.amdhsa_float_round_mode_32 0
		.amdhsa_float_round_mode_16_64 0
		.amdhsa_float_denorm_mode_32 3
		.amdhsa_float_denorm_mode_16_64 3
		.amdhsa_dx10_clamp 1
		.amdhsa_ieee_mode 1
		.amdhsa_fp16_overflow 0
		.amdhsa_tg_split 0
		.amdhsa_exception_fp_ieee_invalid_op 0
		.amdhsa_exception_fp_denorm_src 0
		.amdhsa_exception_fp_ieee_div_zero 0
		.amdhsa_exception_fp_ieee_overflow 0
		.amdhsa_exception_fp_ieee_underflow 0
		.amdhsa_exception_fp_ieee_inexact 0
		.amdhsa_exception_int_div_zero 0
	.end_amdhsa_kernel

amdhsa.kernels:
  - .agpr_count:     0
    .args:
      - .offset:         0
        .size:           184
        .value_kind:     by_value
      - .offset:         184
        .size:           4
        .value_kind:     hidden_block_count_x
      - .offset:         188
        .size:           4
        .value_kind:     hidden_block_count_y
      - .offset:         192
        .size:           4
        .value_kind:     hidden_block_count_z
      - .offset:         196
        .size:           2
        .value_kind:     hidden_group_size_x
      - .offset:         198
        .size:           2
        .value_kind:     hidden_group_size_y
      - .offset:         200
        .size:           2
        .value_kind:     hidden_group_size_z
      - .offset:         202
        .size:           2
        .value_kind:     hidden_remainder_x
      - .offset:         204
        .size:           2
        .value_kind:     hidden_remainder_y
      - .offset:         206
        .size:           2
        .value_kind:     hidden_remainder_z
      - .offset:         224
        .size:           8
        .value_kind:     hidden_global_offset_x
      - .offset:         232
        .size:           8
        .value_kind:     hidden_global_offset_y
      - .offset:         240
        .size:           8
        .value_kind:     hidden_global_offset_z
      - .offset:         248
        .size:           2
        .value_kind:     hidden_grid_dims
      - .offset:         304
        .size:           4
        .value_kind:     hidden_dynamic_lds_size
    .group_segment_fixed_size: 0
    .kernarg_segment_align: 8
    .kernarg_segment_size: 440
    .language:       OpenCL C
    .language_version:
      - 2
      - 0
    .max_flat_workgroup_size: 512
    .name:           _Z3fwd4Args
    .private_segment_fixed_size: 0
    .sgpr_count:     108
    .sgpr_spill_count: 311
    .symbol:         _Z3fwd4Args.kd
    .uniform_work_group_size: 1
    .uses_dynamic_stack: false
    .vgpr_count:     256
    .vgpr_spill_count: 0
    .wavefront_size: 64
